# full-tile attention loops: interleaved max trees, lane-swap index hoisted, shorter MFMA-to-VALU nop
# speedup vs baseline: 1.0222x; 1.0057x over previous
.Lprio_skip:
	v_xor_b32_e32 v223, 32, v242
	v_lshlrev_b32_e32 v223, 2, v223

.LBB0_719:
	s_mul_i32 s26, s64, 0x5400
	v_add_u32_e32 v2, s26, v205
	s_waitcnt lgkmcnt(3)
	ds_read_b128 v[4:7], v2
	s_waitcnt lgkmcnt(1)
	ds_read_b128 v[8:11], v2 offset:32
	ds_read_b128 v[12:15], v2 offset:6656
	ds_read_b128 v[82:85], v2 offset:6688
	ds_read_b128 v[158:161], v2 offset:64
	ds_read_b128 v[162:165], v2 offset:96
	ds_read_b128 v[86:89], v2 offset:6720
	ds_read_b128 v[90:93], v2 offset:6752
	ds_read_b128 v[194:197], v2 offset:128
	ds_read_b128 v[208:211], v2 offset:160
	ds_read_b128 v[94:97], v2 offset:6784
	ds_read_b128 v[166:169], v2 offset:6816
	v_add_u32_e32 v2, s26, v206
	s_waitcnt lgkmcnt(9)
	v_mfma_f32_32x32x16_bf16 v[66:81], v[12:15], v[134:137], v[50:65]
	s_waitcnt lgkmcnt(8)
	v_mfma_f32_32x32x16_bf16 v[66:81], v[82:85], v[138:141], v[66:81]
	s_waitcnt lgkmcnt(5)
	v_mfma_f32_32x32x16_bf16 v[66:81], v[86:89], v[142:145], v[66:81]
	s_waitcnt lgkmcnt(4)
	v_mfma_f32_32x32x16_bf16 v[66:81], v[90:93], v[146:149], v[66:81]
	s_waitcnt lgkmcnt(1)
	v_mfma_f32_32x32x16_bf16 v[66:81], v[94:97], v[150:153], v[66:81]
	s_waitcnt lgkmcnt(0)
	v_mfma_f32_32x32x16_bf16 v[66:81], v[166:169], v[154:157], v[66:81]
	v_mfma_f32_32x32x16_bf16 v[82:97], v[4:7], v[134:137], v[50:65]
	v_mfma_f32_32x32x16_bf16 v[82:97], v[8:11], v[138:141], v[82:97]
	ds_read_b64_tr_b16 v[174:175], v2 offset:13312
	ds_read_b64_tr_b16 v[176:177], v2 offset:13824
	ds_read_b64_tr_b16 v[170:171], v2 offset:14336
	ds_read_b64_tr_b16 v[172:173], v2 offset:14848
	ds_read_b64_tr_b16 v[166:167], v2 offset:15360
	ds_read_b64_tr_b16 v[168:169], v2 offset:15872
	ds_read_b64_tr_b16 v[8:9], v2 offset:16384
	ds_read_b64_tr_b16 v[10:11], v2 offset:16896
	v_mfma_f32_32x32x16_bf16 v[82:97], v[158:161], v[142:145], v[82:97]
	v_mfma_f32_32x32x16_bf16 v[82:97], v[162:165], v[146:149], v[82:97]
	ds_read_b64_tr_b16 v[162:163], v2 offset:17408
	ds_read_b64_tr_b16 v[164:165], v2 offset:17920
	ds_read_b64_tr_b16 v[158:159], v2 offset:18432
	ds_read_b64_tr_b16 v[160:161], v2 offset:18944
	ds_read_b64_tr_b16 v[12:13], v2 offset:19456
	ds_read_b64_tr_b16 v[14:15], v2 offset:19968
	ds_read_b64_tr_b16 v[4:5], v2 offset:20480
	ds_read_b64_tr_b16 v[6:7], v2 offset:20992
	v_mfma_f32_32x32x16_bf16 v[82:97], v[194:197], v[150:153], v[82:97]
	v_mfma_f32_32x32x16_bf16 v[82:97], v[208:211], v[154:157], v[82:97]
	s_nop 4
	v_max3_f32 v194, v66, v67, v68
	v_max3_f32 v196, v69, v70, v71
	v_max3_f32 v194, v194, v72, v73
	v_max3_f32 v196, v196, v74, v75
	v_max3_f32 v194, v194, v76, v77
	v_max3_f32 v196, v196, v78, v79
	v_max3_f32 v194, v194, v196, v80
	v_max3_f32 v2, v82, v83, v84
	v_max3_f32 v195, v85, v86, v87
	v_max3_f32 v2, v2, v88, v89
	v_max3_f32 v195, v195, v90, v91
	v_max3_f32 v2, v2, v92, v93
	v_max3_f32 v195, v195, v94, v95
	v_max3_f32 v2, v2, v195, v96
	v_max_f32_e32 v195, v97, v81
	v_max3_f32 v2, v2, v194, v195
	ds_bpermute_b32 v194, v223, v2
	s_cmp_lg_u32 s73, 0
	s_waitcnt lgkmcnt(0)
	v_max_f32_e32 v208, v2, v194
	s_cbranch_scc0 .Lmla_f_first
	v_cmp_lt_f32_e32 vcc, s81, v208
	s_cbranch_vccz .LBB0_726
	v_max_f32_e32 v2, v208, v208
	v_max_f32_e32 v2, 0, v2
	s_branch .Lmla_f_resc

.LBB0_726:
	v_exp_f32_e32 v2, v82
	v_exp_f32_e32 v208, v66
	v_exp_f32_e32 v66, v83
	v_exp_f32_e32 v209, v67
	v_exp_f32_e32 v67, v84
	v_exp_f32_e32 v84, v68
	v_exp_f32_e32 v68, v85
	v_exp_f32_e32 v85, v69
	v_exp_f32_e32 v69, v86
	v_exp_f32_e32 v86, v70
	v_exp_f32_e32 v70, v87
	v_exp_f32_e32 v87, v71
	v_exp_f32_e32 v71, v88
	v_exp_f32_e32 v88, v72
	v_exp_f32_e32 v72, v89
	v_cvt_pk_bf16_f32 v194, v2, v66
	v_cvt_pk_bf16_f32 v195, v67, v68
	v_cvt_pk_bf16_f32 v196, v69, v70
	v_cvt_pk_bf16_f32 v197, v71, v72
	v_exp_f32_e32 v89, v73
	v_exp_f32_e32 v73, v90
	v_mfma_f32_32x32x16_bf16 v[34:49], v[174:177], v[194:197], v[34:49]
	v_exp_f32_e32 v90, v74
	v_exp_f32_e32 v74, v91
	v_exp_f32_e32 v91, v75
	v_exp_f32_e32 v75, v92
	v_exp_f32_e32 v82, v93
	v_exp_f32_e32 v83, v94
	v_exp_f32_e32 v94, v95
	v_mfma_f32_32x32x16_bf16 v[18:33], v[162:165], v[194:197], v[18:33]
	v_exp_f32_e32 v93, v96
	v_exp_f32_e32 v92, v97
	v_cvt_pk_bf16_f32 v174, v73, v74
	v_cvt_pk_bf16_f32 v175, v75, v82
	v_cvt_pk_bf16_f32 v176, v83, v94
	v_cvt_pk_bf16_f32 v177, v93, v92
	v_exp_f32_e32 v95, v76
	v_exp_f32_e32 v77, v77
	v_mfma_f32_32x32x16_bf16 v[34:49], v[170:173], v[174:177], v[34:49]
	v_cvt_pk_bf16_f32 v170, v208, v209
	v_cvt_pk_bf16_f32 v171, v84, v85
	v_cvt_pk_bf16_f32 v172, v86, v87
	v_cvt_pk_bf16_f32 v173, v88, v89
	v_exp_f32_e32 v76, v78
	v_exp_f32_e32 v96, v79
	v_exp_f32_e32 v79, v80
	v_mfma_f32_32x32x16_bf16 v[18:33], v[158:161], v[174:177], v[18:33]
	v_exp_f32_e32 v78, v81
	s_and_b64 vcc, exec, s[10:11]
	v_mfma_f32_32x32x16_bf16 v[34:49], v[166:169], v[170:173], v[34:49]
	v_cvt_pk_bf16_f32 v166, v90, v91
	v_cvt_pk_bf16_f32 v167, v95, v77
	v_cvt_pk_bf16_f32 v168, v76, v96
	v_cvt_pk_bf16_f32 v169, v79, v78
	v_mfma_f32_32x32x16_bf16 v[18:33], v[12:15], v[170:173], v[18:33]
	s_nop 0
	v_mfma_f32_32x32x16_bf16 v[34:49], v[8:11], v[166:169], v[34:49]
	v_mfma_f32_32x32x16_bf16 v[18:33], v[4:7], v[166:169], v[18:33]
	s_cbranch_vccnz .LBB0_695
	v_mov_b32_e32 v16, v223
	v_mov_b32_e32 v17, 64
	s_mov_b64 s[28:29], -1
	s_mov_b64 s[10:11], 0
	s_cmp_lt_i32 s70, 1
	s_mov_b64 s[26:27], 0
	s_cbranch_scc0 .LBB0_732
	s_and_b64 vcc, exec, s[28:29]
	s_cbranch_vccnz .LBB0_735

.LBB0_835:
	s_waitcnt vmcnt(24)
	v_fma_f32 v116, v116, v120, 0
	v_fmac_f32_e32 v116, v117, v121
	v_fmac_f32_e32 v116, v118, v122
	v_fmac_f32_e32 v116, v119, v123
	v_fmac_f32_e32 v116, v100, v104
	v_fmac_f32_e32 v116, v101, v105
	v_fmac_f32_e32 v116, v102, v106
	v_fmac_f32_e32 v116, v103, v107
	s_waitcnt vmcnt(16)
	v_fma_f32 v120, v124, v128, 0
	v_fmac_f32_e32 v116, v84, v88
	v_fmac_f32_e32 v120, v125, v129
	v_fmac_f32_e32 v116, v85, v89
	v_fmac_f32_e32 v120, v126, v130
	v_fmac_f32_e32 v116, v86, v90
	v_fmac_f32_e32 v120, v127, v131
	v_fmac_f32_e32 v116, v87, v91
	v_fmac_f32_e32 v120, v108, v112
	v_fmac_f32_e32 v116, v52, v60
	v_and_b32_e32 v200, 31, v2
	v_lshlrev_b32_e32 v134, 4, v2
	v_and_b32_e32 v135, 16, v2
	v_lshlrev_b32_e32 v2, 2, v2
	v_fmac_f32_e32 v120, v109, v113
	v_fmac_f32_e32 v116, v53, v61
	v_lshrrev_b32_e32 v132, 5, v132
	v_and_or_b32 v2, v2, 12, v135
	v_fmac_f32_e32 v120, v110, v114
	v_fmac_f32_e32 v116, v54, v62
	v_lshlrev_b32_e32 v133, 8, v132
	v_and_b32_e32 v134, 0xc0, v134
	v_lshlrev_b32_e32 v2, 1, v2
	v_readlane_b32 s4, v255, 27
	v_fmac_f32_e32 v120, v111, v115
	v_fmac_f32_e32 v116, v55, v63
	v_or3_b32 v201, v133, v134, v2
	v_cvt_f32_u32_e32 v2, s4
	v_fmac_f32_e32 v120, v92, v96
	s_waitcnt vmcnt(8)
	v_fmac_f32_e32 v116, v56, v68
	v_fmac_f32_e32 v120, v93, v97
	v_fmac_f32_e32 v116, v57, v69
	v_fmac_f32_e32 v120, v94, v98
	v_fmac_f32_e32 v116, v58, v70
	v_fmac_f32_e32 v120, v95, v99
	v_fmac_f32_e32 v116, v59, v71
	v_mul_f32_e32 v2, 0xbe99999a, v2
	v_fmac_f32_e32 v120, v64, v76
	v_fmac_f32_e32 v116, v36, v40
	v_mul_f32_e32 v133, 0x3fb8aa3b, v2
	s_mov_b32 s0, 0x3fb8aa3b
	v_fmac_f32_e32 v120, v65, v77
	v_fmac_f32_e32 v116, v37, v41
	v_fma_f32 v134, v2, s0, -v133
	v_rndne_f32_e32 v135, v133
	v_fmac_f32_e32 v120, v66, v78
	v_fmac_f32_e32 v116, v38, v42
	v_fmac_f32_e32 v134, 0x32a5705f, v2
	v_sub_f32_e32 v133, v133, v135
	v_fmac_f32_e32 v120, v67, v79
	v_fmac_f32_e32 v116, v39, v43
	v_add_f32_e32 v133, v133, v134
	s_waitcnt vmcnt(0)
	v_fmac_f32_e32 v120, v72, v80
	v_fmac_f32_e32 v116, v20, v24
	v_exp_f32_e32 v133, v133
	v_cvt_i32_f32_e32 v134, v135
	v_fmac_f32_e32 v120, v73, v81
	v_fmac_f32_e32 v116, v21, v25
	v_fmac_f32_e32 v120, v74, v82
	v_fmac_f32_e32 v116, v22, v26
	v_fmac_f32_e32 v120, v75, v83
	v_fmac_f32_e32 v116, v23, v27
	s_mov_b32 s1, 0xc2ce8ed0
	v_fmac_f32_e32 v120, v44, v48
	v_fmac_f32_e32 v116, v4, v8
	v_ldexp_f32 v133, v133, v134
	v_cmp_ngt_f32_e32 vcc, s1, v2
	s_mov_b32 s2, 0x42b17218
	v_fmac_f32_e32 v120, v45, v49
	v_fmac_f32_e32 v116, v5, v9
	v_cndmask_b32_e32 v133, 0, v133, vcc
	v_cmp_nlt_f32_e32 vcc, s2, v2
	v_fmac_f32_e32 v120, v46, v50
	v_fmac_f32_e32 v116, v6, v10
	v_mul_u32_u24_e32 v4, 0x90, v200
	v_cndmask_b32_e32 v2, v246, v133, vcc
	v_fmac_f32_e32 v120, v47, v51
	v_fmac_f32_e32 v116, v7, v11
	v_lshl_add_u32 v207, v132, 4, v4
	v_mov_b32_e32 v4, 0x3f4ccccd
	v_fmac_f32_e32 v120, v28, v32
	v_fmamk_f32 v4, v2, 0xbf19999a, v4
	v_mul_f32_e32 v2, 0x3fb8aa3b, v116
	v_fmac_f32_e32 v120, v29, v33
	v_fma_f32 v5, v116, s0, -v2
	v_rndne_f32_e32 v6, v2
	v_fmac_f32_e32 v120, v30, v34
	v_fmac_f32_e32 v5, 0x32a5705f, v116
	v_sub_f32_e32 v2, v2, v6
	v_fmac_f32_e32 v120, v31, v35
	v_add_f32_e32 v2, v2, v5
	v_fmac_f32_e32 v120, v12, v16
	v_exp_f32_e32 v2, v2
	v_cvt_i32_f32_e32 v5, v6
	v_fmac_f32_e32 v120, v13, v17
	v_fmac_f32_e32 v120, v14, v18
	v_fmac_f32_e32 v120, v15, v19
	v_ldexp_f32 v2, v2, v5
	v_mul_f32_e32 v5, 0x3fb8aa3b, v120
	v_fma_f32 v6, v120, s0, -v5
	v_rndne_f32_e32 v7, v5
	v_fmac_f32_e32 v6, 0x32a5705f, v120
	v_sub_f32_e32 v5, v5, v7
	v_add_f32_e32 v5, v5, v6
	v_exp_f32_e32 v5, v5
	v_cvt_i32_f32_e32 v6, v7
	v_cmp_ngt_f32_e32 vcc, s1, v116
	s_lshl_b32 s12, s4, 6
	v_readlane_b32 s5, v255, 28
	v_cndmask_b32_e32 v2, 0, v2, vcc
	v_cmp_nlt_f32_e32 vcc, s2, v116
	v_ldexp_f32 v5, v5, v6
	s_waitcnt vmcnt(6)
	s_barrier
	v_cndmask_b32_e32 v2, v246, v2, vcc
	v_cmp_ngt_f32_e32 vcc, s1, v120
	s_lshl_b32 s1, s8, 5
	s_ashr_i32 s0, s1, 31
	v_cndmask_b32_e32 v5, 0, v5, vcc
	v_cmp_nlt_f32_e32 vcc, s2, v120
	v_writelane_b32 v255, s1, 35
	v_or_b32_e32 v204, s1, v200
	v_mov_b32_e32 v205, s0
	s_lshl_b64 s[0:1], s[12:13], 2
	v_cndmask_b32_e32 v5, v246, v5, vcc
	v_writelane_b32 v255, s0, 36
	v_sub_f32_e32 v2, v2, v5
	v_add_f32_e32 v202, v4, v2
	v_writelane_b32 v255, s1, 37
	v_readlane_b32 s0, v252, 26
	v_lshlrev_b32_e32 v2, 3, v132
	v_lshlrev_b32_e32 v206, 2, v132
	v_writelane_b32 v255, s0, 38
	v_readlane_b32 s0, v252, 18
	s_add_i32 s70, s81, 0x2400
	s_add_i32 s33, s81, 0x2000
	s_mov_b32 s91, 3
	v_sub_f32_e32 v212, 1.0, v4
	v_mov_b32_e32 v203, v202
	v_or_b32_e32 v213, 59, v206
	s_mov_b32 s74, 0
	v_lshlrev_b32_e32 v208, 1, v2
	s_mov_b32 s5, s13
	v_readlane_b32 s14, v252, 28
	v_readlane_b32 s75, v252, 19
	v_writelane_b32 v255, s0, 39
	s_mov_b32 s2, 0
	v_xor_b32_e32 v230, 32, v242
	v_lshlrev_b32_e32 v230, 2, v230
	s_branch .LBB0_837

.LBB0_851:
	s_mul_i32 s2, s74, 0x4400
	s_add_i32 s6, s2, 0
	v_add_u32_e32 v5, s6, v207
	ds_read_b128 v[6:9], v5 offset:4608
	ds_read_b128 v[10:13], v5
	ds_read_b128 v[14:17], v5 offset:32
	ds_read_b128 v[146:149], v5 offset:4640
	s_cmp_lg_u32 s10, 0
	s_cselect_b64 s[2:3], -1, 0
	s_waitcnt lgkmcnt(2)
	v_mfma_f32_32x32x16_bf16 v[130:145], v[10:13], v[178:181], v[98:113]
	s_and_b64 vcc, exec, s[2:3]
	v_mfma_f32_32x32x16_bf16 v[114:129], v[6:9], v[178:181], v[98:113]
	s_waitcnt lgkmcnt(1)
	v_mfma_f32_32x32x16_bf16 v[130:145], v[14:17], v[182:185], v[130:145]
	s_waitcnt lgkmcnt(0)
	v_mfma_f32_32x32x16_bf16 v[114:129], v[146:149], v[182:185], v[114:129]
	s_nop 9
	v_max3_f32 v2, v130, v131, v132
	v_max3_f32 v8, v133, v134, v135
	v_max3_f32 v6, v114, v115, v116
	v_max3_f32 v7, v117, v118, v119
	v_max3_f32 v2, v2, v136, v137
	v_max3_f32 v8, v8, v138, v139
	v_max3_f32 v6, v6, v120, v121
	v_max3_f32 v7, v7, v122, v123
	v_max3_f32 v2, v2, v140, v141
	v_max3_f32 v8, v8, v142, v143
	v_max3_f32 v6, v6, v124, v125
	v_max3_f32 v7, v7, v126, v127
	v_max3_f32 v2, v2, v8, v144
	v_max3_f32 v6, v6, v7, v128
	v_max_f32_e32 v7, v145, v129
	v_max3_f32 v2, v2, v6, v7
	ds_bpermute_b32 v6, v230, v2
	s_waitcnt lgkmcnt(0)
	v_max_f32_e32 v6, v2, v6
	s_cbranch_vccz .Ldf0_first
	v_cmp_lt_f32_e32 vcc, s11, v6
	s_cbranch_vccz .LBB0_858
	v_max_f32_e32 v2, v6, v6
	v_max_f32_e32 v2, 0, v2
	s_branch .Ldf0_resc

.LBB0_858:
	ds_read_b128 v[6:9], v5 offset:64
	ds_read_b128 v[10:13], v5 offset:96
	ds_read_b128 v[14:17], v5 offset:4672
	ds_read_b128 v[194:197], v5 offset:4704
	s_waitcnt lgkmcnt(3)
	v_mfma_f32_32x32x16_bf16 v[162:177], v[6:9], v[186:189], v[82:97]
	s_and_b64 vcc, exec, s[2:3]
	s_waitcnt lgkmcnt(1)
	v_mfma_f32_32x32x16_bf16 v[146:161], v[14:17], v[186:189], v[82:97]
	v_mfma_f32_32x32x16_bf16 v[162:177], v[10:13], v[190:193], v[162:177]
	s_waitcnt lgkmcnt(0)
	v_mfma_f32_32x32x16_bf16 v[146:161], v[194:197], v[190:193], v[146:161]
	s_nop 9
	v_max3_f32 v2, v162, v163, v164
	v_max3_f32 v7, v165, v166, v167
	v_max3_f32 v5, v146, v147, v148
	v_max3_f32 v6, v149, v150, v151
	v_max3_f32 v2, v2, v168, v169
	v_max3_f32 v7, v7, v170, v171
	v_max3_f32 v5, v5, v152, v153
	v_max3_f32 v6, v6, v154, v155
	v_max3_f32 v2, v2, v172, v173
	v_max3_f32 v7, v7, v174, v175
	v_max3_f32 v5, v5, v156, v157
	v_max3_f32 v6, v6, v158, v159
	v_max3_f32 v2, v2, v7, v176
	v_max3_f32 v5, v5, v6, v160
	v_max_f32_e32 v6, v177, v161
	v_max3_f32 v2, v2, v5, v6
	ds_bpermute_b32 v4, v230, v2
	s_waitcnt lgkmcnt(0)
	v_max_f32_e32 v4, v2, v4
	s_cbranch_vccz .Ldf1_first
	v_cmp_lt_f32_e32 vcc, s11, v4
	s_cbranch_vccz .LBB0_839
	v_max_f32_e32 v2, v4, v4
	v_max_f32_e32 v2, 0, v2
	s_branch .Ldf1_resc
